# gcn layer-2 fast path: loop front (gather index and coefficient fragment per 16-edge batch) rewritten by hand with scalar branches, ds_read2_b32 and unsigned range compares; s_nop per tile removed
# speedup vs baseline: 1.0278x; 1.0088x over previous
.LBB5_16:
	v_cmp_ne_u32_e32 vcc, 0, v1
	v_lshlrev_b32_e32 v87, 4, v79
	v_add_u32_e32 v66, 0x5900, v3
	v_and_b32_e32 v85, 63, v78
	v_and_b32_e32 v86, 15, v78
	v_bfe_u32 v83, v78, 4, 2
	s_cbranch_vccz .LBB5_42
	v_sub_u32_e32 v0, v65, v64
	v_or_b32_e32 v88, v87, v86
	v_add_u32_e32 v91, v0, v2
	v_lshlrev_b32_e32 v90, 2, v88
	ds_read_b32 v84, v90 offset:22528
	v_add_u32_e32 v0, 15, v91
	v_ashrrev_i32_e32 v92, 4, v0
	v_add_u32_e32 v0, 2, v92
	v_ashrrev_i32_e32 v93, 1, v0
	v_cmp_gt_i32_e32 vcc, 1, v93
	v_lshlrev_b32_e32 v89, 2, v83
	s_and_saveexec_b64 s[4:5], vcc
	s_xor_b64 s[4:5], exec, s[4:5]
	v_lshlrev_b32_e32 v89, 2, v83
	s_or_saveexec_b64 s[6:7], s[4:5]
	v_mov_b32_e32 v3, 0
	v_mov_b32_e32 v2, v3
	v_mov_b32_e32 v1, v3
	v_mov_b32_e32 v0, v3
	v_mov_b32_e32 v7, v3
	v_mov_b32_e32 v6, v3
	v_mov_b32_e32 v5, v3
	v_mov_b32_e32 v4, v3
	v_mov_b32_e32 v11, v3
	v_mov_b32_e32 v10, v3
	v_mov_b32_e32 v9, v3
	v_mov_b32_e32 v8, v3
	v_mov_b32_e32 v15, v3
	v_mov_b32_e32 v14, v3
	v_mov_b32_e32 v13, v3
	v_mov_b32_e32 v12, v3
	v_mov_b32_e32 v19, v3
	v_mov_b32_e32 v18, v3
	v_mov_b32_e32 v17, v3
	v_mov_b32_e32 v16, v3
	v_mov_b32_e32 v23, v3
	v_mov_b32_e32 v22, v3
	v_mov_b32_e32 v21, v3
	v_mov_b32_e32 v20, v3
	v_mov_b32_e32 v27, v3
	v_mov_b32_e32 v26, v3
	v_mov_b32_e32 v25, v3
	v_mov_b32_e32 v24, v3
	v_mov_b32_e32 v31, v3
	v_mov_b32_e32 v30, v3
	v_mov_b32_e32 v29, v3
	v_mov_b32_e32 v28, v3
	s_xor_b64 exec, exec, s[6:7]
	s_cbranch_execz .LBB5_44
	v_lshlrev_b32_e32 v0, 4, v85
	v_mov_b32_e32 v1, 0
	v_lshl_add_u64 v[2:3], s[12:13], 0, v[0:1]
	s_movk_i32 s4, 0x1000
	v_lshlrev_b32_e32 v4, 2, v86
	v_add_co_u32_e32 v2, vcc, s4, v2
	global_load_dwordx4 v[32:35], v0, s[12:13]
	global_load_dwordx4 v[36:39], v0, s[12:13] offset:1024
	global_load_dwordx4 v[40:43], v0, s[12:13] offset:2048
	global_load_dwordx4 v[44:47], v0, s[12:13] offset:3072
	v_addc_co_u32_e32 v3, vcc, 0, v3, vcc
	global_load_dword v65, v4, s[14:15]
	global_load_dword v94, v4, s[14:15] offset:64
	global_load_dword v95, v4, s[14:15] offset:128
	global_load_dword v96, v4, s[14:15] offset:192
	global_load_dword v97, v4, s[14:15] offset:256
	global_load_dword v98, v4, s[14:15] offset:320
	global_load_dword v99, v4, s[14:15] offset:384
	global_load_dword v100, v4, s[14:15] offset:448
	global_load_dwordx4 v[48:51], v[2:3], off
	global_load_dwordx4 v[52:55], v[2:3], off offset:1024
	global_load_dwordx4 v[56:59], v[2:3], off offset:2048
	global_load_dwordx4 v[60:63], v[2:3], off offset:3072
	ds_read2st64_b32 v[2:3], v90 offset0:89 offset1:90
	ds_read_b32 v0, v66
	v_cmp_eq_u32_e32 vcc, v89, v86
	v_lshlrev_b32_e32 v4, 3, v82
	s_mov_b32 s4, 0x5040100
	s_mov_b32 s28, 0
	s_waitcnt lgkmcnt(0)
	v_sub_u32_e32 v101, v2, v0
	v_cvt_f16_f32_e32 v2, v84
	v_add_u32_e32 v102, v101, v3
	v_add_u32_e32 v3, s3, v87
	v_sub_u32_e32 v0, v64, v82
	v_or_b32_e32 v103, v3, v86
	v_mov_b32_e32 v3, 0x4400
	v_lshl_add_u32 v104, v0, 3, v3
	v_or_b32_e32 v0, 2, v89
	v_cndmask_b32_e32 v66, 0, v2, vcc
	v_or_b32_e32 v3, 1, v89
	v_cmp_eq_u32_e32 vcc, v0, v86
	s_mov_b64 s[12:13], 0
	s_mov_b32 s29, 0
	v_cndmask_b32_e32 v0, 0, v2, vcc
	v_cmp_eq_u32_e32 vcc, v3, v86
	v_or_b32_e32 v3, 3, v89
	v_mov_b32_e32 v28, v1
	v_cndmask_b32_e32 v67, 0, v2, vcc
	v_cmp_eq_u32_e32 vcc, v3, v86
	v_lshlrev_b32_e32 v3, 3, v86
	v_lshl_add_u32 v3, v64, 3, v3
	v_cndmask_b32_e32 v2, 0, v2, vcc
	v_pack_b32_f16 v105, v0, v2
	v_pack_b32_f16 v0, v67, v0
	v_sub_u32_e32 v3, v3, v4
	v_add_u32_e32 v106, 0x4400, v3
	v_alignbit_b32 v107, v2, v0, 16
	v_perm_b32 v108, v0, v66, s4
	v_mov_b32_e32 v0, v1
	v_mov_b32_e32 v2, v1
	v_mov_b32_e32 v3, v1
	v_mov_b32_e32 v29, v1
	v_mov_b32_e32 v30, v1
	v_mov_b32_e32 v31, v1
	v_mov_b32_e32 v24, v1
	v_mov_b32_e32 v25, v1
	v_mov_b32_e32 v26, v1
	v_mov_b32_e32 v27, v1
	v_mov_b32_e32 v20, v1
	v_mov_b32_e32 v21, v1
	v_mov_b32_e32 v22, v1
	v_mov_b32_e32 v23, v1
	v_mov_b32_e32 v16, v1
	v_mov_b32_e32 v17, v1
	v_mov_b32_e32 v18, v1
	v_mov_b32_e32 v19, v1
	v_mov_b32_e32 v12, v1
	v_mov_b32_e32 v13, v1
	v_mov_b32_e32 v14, v1
	v_mov_b32_e32 v15, v1
	v_mov_b32_e32 v8, v1
	v_mov_b32_e32 v9, v1
	v_mov_b32_e32 v10, v1
	v_mov_b32_e32 v11, v1
	v_mov_b32_e32 v4, v1
	v_mov_b32_e32 v5, v1
	v_mov_b32_e32 v6, v1
	v_mov_b32_e32 v7, v1
	v_and_b32_e32 v109, 48, v78
	v_add_u32_e32 v110, -1, v91
	v_add_u32_e32 v111, -1, v92
	v_pack_b32_f16 v64, v66, v67
	v_readfirstlane_b32 s40, v92
	v_sub_u32_e32 v102, v102, v101
	s_nop 3
	s_branch .LBB5_23
.LBB5_22:
	global_load_dwordx4 v[74:77], v74, s[10:11]
	s_waitcnt vmcnt(1)
	v_mov_b32_e32 v124, v65
	v_mov_b32_e32 v125, v65
	v_mov_b32_e32 v126, v65
	v_mov_b32_e32 v127, v65
	v_add_u32_e32 v93, -1, v93
	s_add_i32 s29, s29, 32
	s_add_i32 s28, s28, 2
	v_cmp_eq_u32_e32 vcc, 0, v93
	v_add_u32_e32 v106, 0x100, v106
	v_mfma_f32_16x16x32_f16 v[112:115], v[70:73], v[32:35], v[124:127]
	s_waitcnt vmcnt(0)
	v_mfma_f32_16x16x32_f16 v[116:119], v[74:77], v[32:35], v[124:127]
	s_nop 1
	s_or_b64 s[12:13], vcc, s[12:13]
	s_nop 1
	v_mov_b32_e32 v124, v94
	v_mov_b32_e32 v125, v94
	v_mov_b32_e32 v126, v94
	v_mov_b32_e32 v127, v94
	v_cvt_pk_f16_f32 v112, v112, v113
	v_cvt_pk_f16_f32 v113, v114, v115
	v_cvt_pk_f16_f32 v114, v116, v117
	v_cvt_pk_f16_f32 v115, v118, v119
	v_mfma_f32_16x16x32_f16 v[116:119], v[74:77], v[36:39], v[124:127]
	v_mfma_f32_16x16x32_f16 v[120:123], v[70:73], v[36:39], v[124:127]
	v_pk_max_f16 v112, v112, 0
	v_pk_max_f16 v113, v113, 0
	v_pk_max_f16 v114, v114, 0
	v_pk_max_f16 v115, v115, 0
	v_mov_b32_e32 v124, v95
	v_mov_b32_e32 v125, v95
	v_mov_b32_e32 v126, v95
	v_mov_b32_e32 v127, v95
	v_mfma_f32_16x16x32_f16 v[28:31], v[112:115], v[66:69], v[28:31]
	v_cvt_pk_f16_f32 v120, v120, v121
	v_cvt_pk_f16_f32 v121, v122, v123
	v_cvt_pk_f16_f32 v122, v116, v117
	v_cvt_pk_f16_f32 v123, v118, v119
	v_mfma_f32_16x16x32_f16 v[116:119], v[74:77], v[40:43], v[124:127]
	v_mfma_f32_16x16x32_f16 v[112:115], v[70:73], v[40:43], v[124:127]
	v_pk_max_f16 v120, v120, 0
	v_pk_max_f16 v121, v121, 0
	v_pk_max_f16 v122, v122, 0
	v_pk_max_f16 v123, v123, 0
	v_mov_b32_e32 v124, v96
	v_mov_b32_e32 v125, v96
	v_mov_b32_e32 v126, v96
	v_mov_b32_e32 v127, v96
	v_mfma_f32_16x16x32_f16 v[24:27], v[120:123], v[66:69], v[24:27]
	v_cvt_pk_f16_f32 v112, v112, v113
	v_cvt_pk_f16_f32 v113, v114, v115
	v_cvt_pk_f16_f32 v114, v116, v117
	v_cvt_pk_f16_f32 v115, v118, v119
	v_mfma_f32_16x16x32_f16 v[116:119], v[74:77], v[44:47], v[124:127]
	v_mfma_f32_16x16x32_f16 v[120:123], v[70:73], v[44:47], v[124:127]
	v_pk_max_f16 v112, v112, 0
	v_pk_max_f16 v113, v113, 0
	v_pk_max_f16 v114, v114, 0
	v_pk_max_f16 v115, v115, 0
	v_mov_b32_e32 v124, v97
	v_mov_b32_e32 v125, v97
	v_mov_b32_e32 v126, v97
	v_mov_b32_e32 v127, v97
	v_mfma_f32_16x16x32_f16 v[20:23], v[112:115], v[66:69], v[20:23]
	v_cvt_pk_f16_f32 v120, v120, v121
	v_cvt_pk_f16_f32 v121, v122, v123
	v_cvt_pk_f16_f32 v122, v116, v117
	v_cvt_pk_f16_f32 v123, v118, v119
	v_mfma_f32_16x16x32_f16 v[116:119], v[74:77], v[48:51], v[124:127]
	v_mfma_f32_16x16x32_f16 v[112:115], v[70:73], v[48:51], v[124:127]
	v_pk_max_f16 v120, v120, 0
	v_pk_max_f16 v121, v121, 0
	v_pk_max_f16 v122, v122, 0
	v_pk_max_f16 v123, v123, 0
	v_mov_b32_e32 v124, v98
	v_mov_b32_e32 v125, v98
	v_mov_b32_e32 v126, v98
	v_mov_b32_e32 v127, v98
	v_mfma_f32_16x16x32_f16 v[16:19], v[120:123], v[66:69], v[16:19]
	v_cvt_pk_f16_f32 v112, v112, v113
	v_cvt_pk_f16_f32 v113, v114, v115
	v_cvt_pk_f16_f32 v114, v116, v117
	v_cvt_pk_f16_f32 v115, v118, v119
	v_mfma_f32_16x16x32_f16 v[116:119], v[74:77], v[52:55], v[124:127]
	v_mfma_f32_16x16x32_f16 v[120:123], v[70:73], v[52:55], v[124:127]
	v_pk_max_f16 v112, v112, 0
	v_pk_max_f16 v113, v113, 0
	v_pk_max_f16 v114, v114, 0
	v_pk_max_f16 v115, v115, 0
	v_mov_b32_e32 v124, v99
	v_mov_b32_e32 v125, v99
	v_mov_b32_e32 v126, v99
	v_mov_b32_e32 v127, v99
	v_mfma_f32_16x16x32_f16 v[12:15], v[112:115], v[66:69], v[12:15]
	v_cvt_pk_f16_f32 v120, v120, v121
	v_cvt_pk_f16_f32 v121, v122, v123
	v_cvt_pk_f16_f32 v122, v116, v117
	v_cvt_pk_f16_f32 v123, v118, v119
	v_mfma_f32_16x16x32_f16 v[116:119], v[74:77], v[56:59], v[124:127]
	v_mfma_f32_16x16x32_f16 v[112:115], v[70:73], v[56:59], v[124:127]
	v_pk_max_f16 v120, v120, 0
	v_pk_max_f16 v121, v121, 0
	v_pk_max_f16 v122, v122, 0
	v_pk_max_f16 v123, v123, 0
	v_mov_b32_e32 v124, v100
	v_mov_b32_e32 v125, v100
	v_mov_b32_e32 v126, v100
	v_mov_b32_e32 v127, v100
	v_mfma_f32_16x16x32_f16 v[8:11], v[120:123], v[66:69], v[8:11]
	v_cvt_pk_f16_f32 v112, v112, v113
	v_cvt_pk_f16_f32 v113, v114, v115
	v_cvt_pk_f16_f32 v114, v116, v117
	v_cvt_pk_f16_f32 v115, v118, v119
	v_mfma_f32_16x16x32_f16 v[116:119], v[74:77], v[60:63], v[124:127]
	v_mfma_f32_16x16x32_f16 v[120:123], v[70:73], v[60:63], v[124:127]
	v_pk_max_f16 v112, v112, 0
	v_pk_max_f16 v113, v113, 0
	v_pk_max_f16 v114, v114, 0
	v_pk_max_f16 v115, v115, 0
	s_nop 3
	v_mfma_f32_16x16x32_f16 v[4:7], v[112:115], v[66:69], v[4:7]
	v_cvt_pk_f16_f32 v120, v120, v121
	v_cvt_pk_f16_f32 v121, v122, v123
	v_cvt_pk_f16_f32 v122, v116, v117
	v_cvt_pk_f16_f32 v123, v118, v119
	v_pk_max_f16 v120, v120, 0
	v_pk_max_f16 v121, v121, 0
	v_pk_max_f16 v122, v122, 0
	v_pk_max_f16 v123, v123, 0
	s_nop 1
	v_mfma_f32_16x16x32_f16 v[0:3], v[120:123], v[66:69], v[0:3]
	s_andn2_b64 exec, exec, s[12:13]
	s_cbranch_execz .LBB5_43
.LBB5_23:
	s_cmp_lt_i32 s28, s40
	s_cbranch_scc1 .Lg2f_b0_gen
	s_cmp_eq_u32 s28, s40
	s_cbranch_scc1 .Lg2f_b0_self
	v_mov_b32_e32 v66, 0
	v_mov_b32_e32 v67, 0
	v_mov_b32_e32 v68, s3
	s_branch .Lg2f_b0_done
.Lg2f_b0_self:
	v_mov_b32_e32 v66, v108
	v_mov_b32_e32 v67, v107
	v_mov_b32_e32 v68, v103
	s_branch .Lg2f_b0_done
.Lg2f_b0_gen:
	v_add_u32_e32 v112, s29, v86
	v_add_u32_e32 v113, s29, v89
	v_min_i32_e32 v112, v112, v110
	v_lshl_add_u32 v114, v113, 3, v104
	v_lshl_add_u32 v112, v112, 3, v104
	ds_read2_b32 v[116:117], v114 offset0:1 offset1:3
	ds_read2_b32 v[118:119], v114 offset0:5 offset1:7
	ds_read_b32 v68, v112
	v_sub_u32_e32 v113, v113, v101
	v_add_u32_e32 v114, 1, v113
	v_add_u32_e32 v115, 2, v113
	v_add_u32_e32 v120, 3, v113
	v_cmp_gt_u32_e64 s[42:43], v102, v113
	v_cmp_gt_u32_e64 s[44:45], v102, v114
	v_cmp_gt_u32_e64 s[46:47], v102, v115
	v_cmp_gt_u32_e64 s[48:49], v102, v120
	s_waitcnt lgkmcnt(1)
	v_cvt_f16_f32_e32 v116, v116
	v_cvt_f16_f32_e32 v117, v117
	v_cvt_f16_f32_e32 v118, v118
	v_cvt_f16_f32_e32 v119, v119
	v_cndmask_b32_e64 v116, 0, v116, s[42:43]
	v_cndmask_b32_e64 v117, 0, v117, s[44:45]
	v_cndmask_b32_e64 v118, 0, v118, s[46:47]
	v_cndmask_b32_e64 v119, 0, v119, s[48:49]
	v_pack_b32_f16 v66, v116, v117
	v_pack_b32_f16 v67, v118, v119
	s_waitcnt lgkmcnt(0)
.Lg2f_b0_done:
	v_lshl_or_b32 v68, v68, 6, v109
	global_load_dwordx4 v[70:73], v68, s[10:11]
	s_add_i32 s41, s28, 1
	s_cmp_lt_i32 s41, s40
	s_cbranch_scc1 .Lg2f_b1_gen
	s_cmp_eq_u32 s41, s40
	s_cbranch_scc1 .Lg2f_b1_self
	v_mov_b32_e32 v68, 0
	v_mov_b32_e32 v69, 0
	v_mov_b32_e32 v74, s3
	s_branch .Lg2f_b1_done
.Lg2f_b1_self:
	v_mov_b32_e32 v68, v64
	v_mov_b32_e32 v69, v105
	v_mov_b32_e32 v74, v103
	s_branch .Lg2f_b1_done
.Lg2f_b1_gen:
	s_add_i32 s41, s29, 16
	v_add_u32_e32 v112, s41, v86
	v_add_u32_e32 v113, s41, v89
	v_min_i32_e32 v112, v112, v110
	v_lshl_add_u32 v114, v113, 3, v104
	v_lshl_add_u32 v112, v112, 3, v104
	ds_read2_b32 v[116:117], v114 offset0:1 offset1:3
	ds_read2_b32 v[118:119], v114 offset0:5 offset1:7
	ds_read_b32 v74, v112
	v_sub_u32_e32 v113, v113, v101
	v_add_u32_e32 v114, 1, v113
	v_add_u32_e32 v115, 2, v113
	v_add_u32_e32 v120, 3, v113
	v_cmp_gt_u32_e64 s[42:43], v102, v113
	v_cmp_gt_u32_e64 s[44:45], v102, v114
	v_cmp_gt_u32_e64 s[46:47], v102, v115
	v_cmp_gt_u32_e64 s[48:49], v102, v120
	s_waitcnt lgkmcnt(1)
	v_cvt_f16_f32_e32 v116, v116
	v_cvt_f16_f32_e32 v117, v117
	v_cvt_f16_f32_e32 v118, v118
	v_cvt_f16_f32_e32 v119, v119
	v_cndmask_b32_e64 v116, 0, v116, s[42:43]
	v_cndmask_b32_e64 v117, 0, v117, s[44:45]
	v_cndmask_b32_e64 v118, 0, v118, s[46:47]
	v_cndmask_b32_e64 v119, 0, v119, s[48:49]
	v_pack_b32_f16 v68, v116, v117
	v_pack_b32_f16 v69, v118, v119
	s_waitcnt lgkmcnt(0)
.Lg2f_b1_done:
	v_lshl_or_b32 v74, v74, 6, v109
	s_branch .LBB5_22
